# code placement: step head +24 bytes, flush head +28 bytes (step 4 mod 16, flush 12 mod 16)
# speedup vs baseline: 1.0004x; 1.0004x over previous
.LBB1_143:
	s_or_b64 exec, exec, s[2:3]
	v_cndmask_b32_e64 v24, v14, 0, s[4:5]
	v_ashrrev_i32_e32 v25, 31, v24
	v_lshlrev_b64 v[24:25], 3, v[24:25]
	s_mov_b64 s[2:3], src_shared_base
	v_lshl_add_u64 v[24:25], s[56:57], 0, v[24:25]
	v_mov_b32_e32 v14, s3
	v_cndmask_b32_e64 v232, v24, 0, s[4:5]
	v_add_lshl_u32 v24, s13, v1, 1
	v_cndmask_b32_e64 v233, v25, v14, s[4:5]
	s_mov_b32 s81, s4
	s_nop 0
	s_nop 0
	s_nop 0
	s_nop 0
	s_nop 0
	s_nop 0
	v_ashrrev_i32_e32 v25, 31, v24
	v_lshl_add_u64 v[24:25], v[24:25], 2, v[232:233]
	flat_load_dwordx2 v[82:83], v[24:25]
	s_mov_b32 s2, 0x4038aa3b
	v_add_f32_e32 v239, s33, v11
	s_waitcnt vmcnt(0)
	v_fma_mixlo_f16 v11, v18, s2, 0
	v_fma_mixlo_f16 v25, v16, s2, 0
	v_fma_mixlo_f16 v27, v17, s2, 0
	v_add_lshl_u32 v22, s13, v22, 1
	v_fma_mixlo_f16 v14, v19, s2, 0
	v_fma_mixlo_f16 v18, v18, s2, -v11 op_sel_hi:[0,0,1]
	v_fma_mixlo_f16 v16, v16, s2, -v25 op_sel_hi:[0,0,1]
	v_fma_mixlo_f16 v17, v17, s2, -v27 op_sel_hi:[0,0,1]
	s_mov_b32 s14, 0x186a0
	v_ashrrev_i32_e32 v23, 31, v22
	v_fma_mixlo_f16 v19, v19, s2, -v14 op_sel_hi:[0,0,1]
	v_cndmask_b32_e64 v11, 0, v11, s[0:1]
	v_cndmask_b32_e64 v14, 0, v14, s[0:1]
	v_cndmask_b32_e64 v25, 0, v25, s[0:1]
	v_cndmask_b32_e64 v27, 0, v27, s[0:1]
	v_cndmask_b32_e64 v18, 0, v18, s[0:1]
	v_cndmask_b32_e64 v16, 0, v16, s[0:1]
	v_cndmask_b32_e64 v17, 0, v17, s[0:1]
	v_pack_b32_f16 v179, v11, v14
	v_pack_b32_f16 v178, v11, v18
	v_pack_b32_f16 v185, v27, v17
	v_pack_b32_f16 v182, v25, v16
	v_lshl_add_u64 v[16:17], v[22:23], 2, v[232:233]
	flat_load_dwordx2 v[236:237], v[16:17]
	v_mov_b32_e32 v17, v2
	v_cndmask_b32_e64 v19, 0, v19, s[0:1]
	v_pack_b32_f16 v180, v19, v14
	v_fma_mixlo_f16 v14, v13, s2, 0
	v_fma_mixlo_f16 v13, v13, s2, -v14 op_sel_hi:[0,0,1]
	v_cndmask_b32_e64 v14, 0, v14, s[0:1]
	v_cndmask_b32_e64 v13, 0, v13, s[0:1]
	v_fma_mixlo_f16 v24, v20, s2, 0
	v_fma_mixlo_f16 v26, v21, s2, 0
	v_or_b32_e32 v240, 64, v1
	v_pack_b32_f16 v188, v13, v14
	v_fma_mixlo_f16 v13, v10, s2, 0
	v_lshl_add_u32 v244, v1, 2, v3
	v_and_b32_e32 v0, 32, v0
	v_mov_b32_e32 v1, 0xa300
	v_fma_mixlo_f16 v20, v20, s2, -v24 op_sel_hi:[0,0,1]
	v_fma_mixlo_f16 v21, v21, s2, -v26 op_sel_hi:[0,0,1]
	v_fma_mixlo_f16 v10, v10, s2, -v13 op_sel_hi:[0,0,1]
	v_lshl_or_b32 v245, v0, 2, v1
	v_lshl_add_u32 v246, v8, 4, v1
	v_add_u32_e32 v3, 64, v7
	v_cndmask_b32_e64 v24, 0, v24, s[0:1]
	v_cndmask_b32_e64 v26, 0, v26, s[0:1]
	v_cndmask_b32_e64 v20, 0, v20, s[0:1]
	v_cndmask_b32_e64 v21, 0, v21, s[0:1]
	v_cndmask_b32_e64 v13, 0, v13, s[0:1]
	v_cndmask_b32_e64 v10, 0, v10, s[0:1]
	v_mov_b32_e32 v0, 0xc0
	v_pack_b32_f16 v183, v25, v26
	v_pack_b32_f16 v181, v24, v20
	v_pack_b32_f16 v184, v21, v26
	v_pack_b32_f16 v193, v13, v10
	v_lshlrev_b32_e32 v251, 3, v9
	v_mov_b32_e32 v7, v2
	v_mov_b32_e32 v9, v2
	v_mov_b32_e32 v10, v2
	v_mov_b32_e32 v13, v2
	v_add_u32_e32 v242, 8, v251
	s_waitcnt lgkmcnt(0)
	v_sub_u32_e32 v234, v231, v230
	s_mov_b64 s[4:5], 0
	v_mov_b32_e32 v249, s6
	s_mov_b32 s71, s6
	v_mov_b32_e32 v231, s13
	s_mov_b32 s70, s13
	s_mov_b32 s15, 0x5040100
	s_mov_b32 s82, 1.0
	s_mov_b32 s83, 1.0
	s_mov_b32 s73, 0x3c000000
	s_mov_b32 s74, 0x42004000
	s_mov_b32 s75, 0x48804800
	s_mov_b32 s76, 0x49804900
	s_mov_b32 s77, 0x4c404c00
	s_mov_b32 s78, 0x4cc04c80
	s_mov_b32 s79, 0x4e404e00
	s_mov_b32 s80, 0x4ec04e80
	v_mov_b32_e32 v197, 0x3c003c00
	s_mov_b32 s16, 0x10000
	s_mov_b32 s17, 0x7a100
	v_lshl_or_b32 v11, v82, 3, 3
	v_cmp_gt_u32_e32 vcc, s14, v82
	v_mov_b32_e32 v196, v83
	s_nop 0
	v_cndmask_b32_e32 v16, 3, v11, vcc
	v_lshl_add_u64 v[16:17], v[16:17], 2, s[54:55]
	global_load_dword v241, v[16:17], off
	v_fma_mixlo_f16 v11, v12, s2, 0
	v_fma_mixlo_f16 v12, v12, s2, -v11 op_sel_hi:[0,0,1]
	v_cndmask_b32_e64 v11, 0, v11, s[0:1]
	v_cndmask_b32_e64 v12, 0, v12, s[0:1]
	v_pack_b32_f16 v187, v11, v14
	v_pack_b32_f16 v186, v11, v12
	v_fma_mixlo_f16 v11, v4, s2, 0
	v_fma_mixlo_f16 v4, v4, s2, -v11 op_sel_hi:[0,0,1]
	v_cndmask_b32_e64 v11, 0, v11, s[0:1]
	v_cndmask_b32_e64 v4, 0, v4, s[0:1]
	v_fma_mixlo_f16 v16, v15, s2, 0
	v_pack_b32_f16 v190, v11, v4
	v_lshrrev_b32_e32 v4, 3, v8
	v_fma_mixlo_f16 v15, v15, s2, -v16 op_sel_hi:[0,0,1]
	v_fma_mixlo_f16 v12, v5, s2, 0
	v_and_b32_e32 v243, 4, v4
	v_cndmask_b32_e64 v16, 0, v16, s[0:1]
	v_cndmask_b32_e64 v15, 0, v15, s[0:1]
	v_fma_mixlo_f16 v5, v5, s2, -v12 op_sel_hi:[0,0,1]
	v_lshl_add_u32 v247, v243, 6, v1
	v_xor_b32_e32 v1, 32, v6
	v_pack_b32_f16 v189, v16, v15
	v_cndmask_b32_e64 v12, 0, v12, s[0:1]
	v_cndmask_b32_e64 v5, 0, v5, s[0:1]
	v_cmp_lt_i32_e32 vcc, v1, v3
	v_mov_b32_e32 v16, v2
	v_mov_b32_e32 v17, v2
	v_pack_b32_f16 v191, v11, v12
	v_pack_b32_f16 v192, v5, v12
	v_lshl_or_b32 v0, v4, 6, v0
	v_cndmask_b32_e32 v1, v6, v1, vcc
	v_mov_b32_e32 v3, v2
	v_mov_b32_e32 v4, v2
	v_mov_b32_e32 v5, v2
	v_mov_b32_e32 v6, v2
	v_mov_b32_e32 v8, v2
	v_mov_b32_e32 v11, v2
	v_mov_b32_e32 v12, v2
	v_mov_b32_e32 v14, v2
	v_mov_b32_e32 v15, v2
	v_mov_b64_e32 v[32:33], v[16:17]
	v_mov_b64_e32 v[48:49], v[16:17]
	v_mov_b64_e32 v[64:65], v[16:17]
	v_mov_b64_e32 v[80:81], v[16:17]
	v_lshlrev_b32_e32 v248, 2, v1
	v_add_u32_e32 v250, 0xa300, v0
	v_mov_b64_e32 v[30:31], v[14:15]
	v_mov_b64_e32 v[28:29], v[12:13]
	v_mov_b64_e32 v[26:27], v[10:11]
	v_mov_b64_e32 v[24:25], v[8:9]
	v_mov_b64_e32 v[22:23], v[6:7]
	v_mov_b64_e32 v[20:21], v[4:5]
	v_mov_b64_e32 v[18:19], v[2:3]
	v_mov_b64_e32 v[46:47], v[14:15]
	v_mov_b64_e32 v[44:45], v[12:13]
	v_mov_b64_e32 v[42:43], v[10:11]
	v_mov_b64_e32 v[40:41], v[8:9]
	v_mov_b64_e32 v[38:39], v[6:7]
	v_mov_b64_e32 v[36:37], v[4:5]
	v_mov_b64_e32 v[34:35], v[2:3]
	v_mov_b64_e32 v[62:63], v[14:15]
	v_mov_b64_e32 v[60:61], v[12:13]
	v_mov_b64_e32 v[58:59], v[10:11]
	v_mov_b64_e32 v[56:57], v[8:9]
	v_mov_b64_e32 v[54:55], v[6:7]
	v_mov_b64_e32 v[52:53], v[4:5]
	v_mov_b64_e32 v[50:51], v[2:3]
	v_mov_b64_e32 v[78:79], v[14:15]
	v_mov_b64_e32 v[76:77], v[12:13]
	v_mov_b64_e32 v[74:75], v[10:11]
	v_mov_b64_e32 v[72:73], v[8:9]
	v_mov_b64_e32 v[70:71], v[6:7]
	v_mov_b64_e32 v[68:69], v[4:5]
	v_mov_b64_e32 v[66:67], v[2:3]
	s_branch .LBB1_145
